# dilated attention: s_setprio 1/0 around each 8-MFMA cluster
# speedup vs baseline: 1.0039x; 1.0012x over previous
.LBB0_336:
	s_waitcnt vmcnt(0)
	s_setprio 1
	v_mfma_f32_32x32x16_bf16 v[50:65], v[126:129], v[66:69], 0
	v_med3_i32 v166, v157, 31, v186
	v_lshl_add_u32 v166, v166, 2, s88
	v_add_u32_e32 v167, 0xffffff84, v166
	v_add_u32_e32 v166, -1, v157
	v_med3_i32 v168, v166, -1, v185
	v_med3_i32 v166, v166, 31, v186
	v_lshl_add_u32 v166, v166, 2, s88
	v_mfma_f32_32x32x16_bf16 v[34:49], v[142:145], v[66:69], 0
	v_add_u32_e32 v192, 0xffffff84, v166
	v_add_u32_e32 v166, -2, v157
	v_lshl_add_u32 v169, v168, 2, s88
	v_med3_i32 v168, v166, -1, v185
	v_med3_i32 v166, v166, 31, v186
	v_lshl_add_u32 v166, v166, 2, s88
	v_add_u32_e32 v194, 0xffffff84, v166
	v_mfma_f32_32x32x16_bf16 v[50:65], v[138:141], v[70:73], v[50:65]
	v_add_u32_e32 v166, -3, v157
	v_med3_i32 v0, v157, -1, v185
	v_lshl_add_u32 v193, v168, 2, s88
	v_med3_i32 v168, v166, -1, v185
	v_med3_i32 v166, v166, 31, v186
	v_lshl_add_u32 v0, v0, 2, s88
	v_lshl_add_u32 v195, v168, 2, s88
	v_mfma_f32_32x32x16_bf16 v[34:49], v[122:125], v[70:73], v[34:49]
	v_lshl_add_u32 v166, v166, 2, s88
	v_add_u32_e32 v196, 0xffffff84, v166
	ds_read_b32 v166, v0 offset:4
	ds_read_b32 v168, v167
	ds_read_b32 v167, v169 offset:4
	ds_read_b32 v169, v192
	ds_read_b32 v192, v193 offset:4
	ds_read_b32 v194, v194
	ds_read_b32 v193, v195 offset:4
	ds_read_b32 v195, v196
	v_add_u32_e32 v0, -8, v157
	v_add_u32_e32 v191, s8, v170
	s_cmp_gt_i32 s8, -1
	v_mfma_f32_32x32x16_bf16 v[50:65], v[118:121], v[74:77], v[50:65]
	v_mfma_f32_32x32x16_bf16 v[34:49], v[134:137], v[74:77], v[34:49]
	v_mfma_f32_32x32x16_bf16 v[50:65], v[130:133], v[78:81], v[50:65]
	v_mfma_f32_32x32x16_bf16 v[34:49], v[114:117], v[78:81], v[34:49]
	s_setprio 0
	s_waitcnt lgkmcnt(0)
	s_nop 9
	v_add_f32_e64 v50, v50, v166
	v_add_f32_e64 v51, v51, v167
	v_pk_add_f32 v[166:167], v[34:35], v[168:169]
	v_pk_add_f32 v[34:35], v[52:53], v[192:193]
	v_add_u32_e32 v53, -9, v157
	v_med3_i32 v168, v53, -1, v185
	v_med3_i32 v53, v53, 31, v186
	v_lshl_add_u32 v53, v53, 2, s88
	v_add_u32_e32 v192, 0xffffff84, v53
	v_add_u32_e32 v53, -10, v157
	v_lshl_add_u32 v169, v168, 2, s88
	v_med3_i32 v168, v53, -1, v185
	v_med3_i32 v53, v53, 31, v186
	v_lshl_add_u32 v53, v53, 2, s88
	v_pk_add_f32 v[36:37], v[36:37], v[194:195]
	v_add_u32_e32 v194, 0xffffff84, v53
	v_add_u32_e32 v53, -11, v157
	v_med3_i32 v52, v0, -1, v185
	v_med3_i32 v0, v0, 31, v186
	v_lshl_add_u32 v193, v168, 2, s88
	v_med3_i32 v168, v53, -1, v185
	v_med3_i32 v53, v53, 31, v186
	v_lshl_add_u32 v52, v52, 2, s88
	v_lshl_add_u32 v0, v0, 2, s88
	v_lshl_add_u32 v195, v168, 2, s88
	v_lshl_add_u32 v53, v53, 2, s88
	v_add_u32_e32 v0, 0xffffff84, v0
	v_add_u32_e32 v196, 0xffffff84, v53
	ds_read_b32 v52, v52 offset:4
	ds_read_b32 v168, v0
	ds_read_b32 v53, v169 offset:4
	ds_read_b32 v169, v192
	ds_read_b32 v192, v193 offset:4
	ds_read_b32 v193, v195 offset:4
	ds_read_b32 v194, v194
	ds_read_b32 v195, v196
	s_waitcnt lgkmcnt(5)
	v_pk_add_f32 v[54:55], v[54:55], v[52:53]
	s_waitcnt lgkmcnt(4)
	v_pk_add_f32 v[52:53], v[38:39], v[168:169]
	s_waitcnt lgkmcnt(2)
	v_pk_add_f32 v[38:39], v[56:57], v[192:193]
	v_subrev_u32_e32 v57, 17, v157
	v_med3_i32 v168, v57, -1, v185
	v_med3_i32 v57, v57, 31, v186
	v_lshl_add_u32 v57, v57, 2, s88
	v_add_u32_e32 v169, 0xffffff84, v57
	v_subrev_u32_e32 v57, 18, v157
	v_med3_i32 v192, v57, -1, v185
	v_med3_i32 v57, v57, 31, v186
	v_lshl_add_u32 v57, v57, 2, s88
	v_add_u32_e32 v0, -16, v157
	v_add_u32_e32 v197, 0xffffff84, v57
	v_subrev_u32_e32 v57, 19, v157
	v_med3_i32 v56, v0, -1, v185
	v_med3_i32 v0, v0, 31, v186
	v_lshl_add_u32 v196, v192, 2, s88
	v_med3_i32 v192, v57, -1, v185
	v_med3_i32 v57, v57, 31, v186
	v_lshl_add_u32 v56, v56, 2, s88
	v_lshl_add_u32 v0, v0, 2, s88
	v_lshl_add_u32 v199, v192, 2, s88
	v_lshl_add_u32 v57, v57, 2, s88
	v_add_u32_e32 v0, 0xffffff84, v0
	v_lshl_add_u32 v168, v168, 2, s88
	v_add_u32_e32 v200, 0xffffff84, v57
	ds_read_b32 v56, v56 offset:4
	ds_read_b32 v192, v0
	ds_read_b32 v57, v168 offset:4
	ds_read_b32 v193, v169
	ds_read_b32 v196, v196 offset:4
	ds_read_b32 v198, v197
	ds_read_b32 v197, v199 offset:4
	ds_read_b32 v199, v200
	s_waitcnt lgkmcnt(5)
	v_pk_add_f32 v[58:59], v[58:59], v[56:57]
	s_waitcnt lgkmcnt(4)
	v_pk_add_f32 v[56:57], v[42:43], v[192:193]
	v_pk_add_f32 v[168:169], v[40:41], v[194:195]
	s_waitcnt lgkmcnt(1)
	v_pk_add_f32 v[40:41], v[60:61], v[196:197]
	s_waitcnt lgkmcnt(0)
	v_pk_add_f32 v[42:43], v[44:45], v[198:199]
	v_subrev_u32_e32 v45, 25, v157
	v_med3_i32 v60, v45, -1, v185
	v_med3_i32 v45, v45, 31, v186
	v_lshl_add_u32 v45, v45, 2, s88
	v_add_u32_e32 v192, 0xffffff84, v45
	v_subrev_u32_e32 v45, 26, v157
	v_lshl_add_u32 v61, v60, 2, s88
	v_med3_i32 v60, v45, -1, v185
	v_med3_i32 v45, v45, 31, v186
	v_lshl_add_u32 v45, v45, 2, s88
	v_subrev_u32_e32 v0, 24, v157
	v_add_u32_e32 v194, 0xffffff84, v45
	v_subrev_u32_e32 v45, 27, v157
	v_med3_i32 v44, v0, -1, v185
	v_med3_i32 v0, v0, 31, v186
	v_lshl_add_u32 v193, v60, 2, s88
	v_med3_i32 v60, v45, -1, v185
	v_med3_i32 v45, v45, 31, v186
	v_lshl_add_u32 v44, v44, 2, s88
	v_lshl_add_u32 v0, v0, 2, s88
	v_lshl_add_u32 v195, v60, 2, s88
	v_lshl_add_u32 v45, v45, 2, s88
	v_add_u32_e32 v0, 0xffffff84, v0
	v_add_u32_e32 v196, 0xffffff84, v45
	ds_read_b32 v44, v44 offset:4
	ds_read_b32 v60, v0
	ds_read_b32 v45, v61 offset:4
	ds_read_b32 v61, v192
	ds_read_b32 v192, v193 offset:4
	ds_read_b32 v193, v195 offset:4
	ds_read_b32 v194, v194
	ds_read_b32 v195, v196
	s_waitcnt lgkmcnt(5)
	v_pk_add_f32 v[62:63], v[62:63], v[44:45]
	s_waitcnt lgkmcnt(4)
	v_pk_add_f32 v[60:61], v[46:47], v[60:61]
	s_waitcnt lgkmcnt(2)
	v_pk_add_f32 v[44:45], v[64:65], v[192:193]
	s_waitcnt lgkmcnt(0)
	v_pk_add_f32 v[46:47], v[48:49], v[194:195]
	s_cbranch_scc1 .LBB0_338
	v_cmp_lt_i32_e32 vcc, -1, v191
	s_nop 1
	v_cndmask_b32_e32 v50, v187, v50, vcc
	v_cmp_lt_i32_e32 vcc, -2, v191
	s_nop 1
	v_cndmask_b32_e32 v51, v187, v51, vcc
	v_cmp_lt_i32_e32 vcc, -3, v191
	s_nop 1
	v_cndmask_b32_e32 v34, v187, v34, vcc
	v_cmp_lt_i32_e32 vcc, -4, v191
	s_nop 1
	v_cndmask_b32_e32 v35, v187, v35, vcc
	v_cmp_lt_i32_e32 vcc, -9, v191
	s_nop 1
	v_cndmask_b32_e32 v54, v187, v54, vcc
	v_cmp_lt_i32_e32 vcc, -10, v191
	s_nop 1
	v_cndmask_b32_e32 v55, v187, v55, vcc
	v_cmp_lt_i32_e32 vcc, -11, v191
	s_nop 1
	v_cndmask_b32_e32 v38, v187, v38, vcc
	v_cmp_lt_i32_e32 vcc, -12, v191
	s_nop 1
	v_cndmask_b32_e32 v39, v187, v39, vcc
	v_cmp_lt_i32_e32 vcc, s53, v191
	s_nop 1
	v_cndmask_b32_e32 v58, v187, v58, vcc
	v_cmp_lt_i32_e32 vcc, s52, v191
	s_nop 1
	v_cndmask_b32_e32 v59, v187, v59, vcc
	v_cmp_lt_i32_e32 vcc, s51, v191
	s_nop 1
	v_cndmask_b32_e32 v40, v187, v40, vcc
	v_cmp_lt_i32_e32 vcc, s50, v191
	s_nop 1
	v_cndmask_b32_e32 v41, v187, v41, vcc
	v_cmp_lt_i32_e32 vcc, s49, v191
	s_nop 1
	v_cndmask_b32_e32 v62, v187, v62, vcc
	v_cmp_lt_i32_e32 vcc, s48, v191
	s_nop 1
	v_cndmask_b32_e32 v63, v187, v63, vcc
	v_cmp_lt_i32_e32 vcc, s47, v191
	s_nop 1
	v_cndmask_b32_e32 v44, v187, v44, vcc
	v_cmp_lt_i32_e32 vcc, s46, v191
	s_nop 1
	v_cndmask_b32_e32 v45, v187, v45, vcc
	v_cmp_lt_i32_e32 vcc, s70, v191
	s_nop 1
	v_cndmask_b32_e32 v166, v187, v166, vcc
	v_cmp_lt_i32_e32 vcc, s69, v191
	s_nop 1
	v_cndmask_b32_e32 v167, v187, v167, vcc
	v_cmp_lt_i32_e32 vcc, s68, v191
	s_nop 1
	v_cndmask_b32_e32 v36, v187, v36, vcc
	v_cmp_lt_i32_e32 vcc, s67, v191
	s_nop 1
	v_cndmask_b32_e32 v37, v187, v37, vcc
	v_cmp_lt_i32_e32 vcc, s66, v191
	s_nop 1
	v_cndmask_b32_e32 v52, v187, v52, vcc
	v_cmp_lt_i32_e32 vcc, s65, v191
	s_nop 1
	v_cndmask_b32_e32 v53, v187, v53, vcc
	v_cmp_lt_i32_e32 vcc, s64, v191
	s_nop 1
	v_cndmask_b32_e32 v168, v187, v168, vcc
	v_cmp_lt_i32_e32 vcc, s63, v191
	s_nop 1
	v_cndmask_b32_e32 v169, v187, v169, vcc
	v_cmp_lt_i32_e32 vcc, s62, v191
	s_nop 1
	v_cndmask_b32_e32 v56, v187, v56, vcc
	v_cmp_lt_i32_e32 vcc, s61, v191
	s_nop 1
	v_cndmask_b32_e32 v57, v187, v57, vcc
	v_cmp_lt_i32_e32 vcc, s60, v191
	s_nop 1
	v_cndmask_b32_e32 v42, v187, v42, vcc
	v_cmp_lt_i32_e32 vcc, s59, v191
	s_nop 1
	v_cndmask_b32_e32 v43, v187, v43, vcc
	v_cmp_lt_i32_e32 vcc, s58, v191
	s_nop 1
	v_cndmask_b32_e32 v60, v187, v60, vcc
	v_cmp_lt_i32_e32 vcc, s57, v191
	s_nop 1
	v_cndmask_b32_e32 v61, v187, v61, vcc
	v_cmp_lt_i32_e32 vcc, s56, v191
	s_nop 1
	v_cndmask_b32_e32 v46, v187, v46, vcc
	v_cmp_lt_i32_e32 vcc, s55, v191
	s_nop 1
	v_cndmask_b32_e32 v47, v187, v47, vcc

.LBB0_342:
	v_sub_f32_e32 v49, v50, v48
	v_sub_f32_e32 v50, v166, v48
	v_sub_f32_e32 v34, v34, v48
	v_exp_f32_e32 v49, v49
	v_exp_f32_e32 v50, v50
	v_sub_f32_e32 v51, v51, v48
	v_sub_f32_e32 v64, v167, v48
	v_exp_f32_e32 v167, v34
	v_sub_f32_e32 v34, v36, v48
	v_exp_f32_e32 v51, v51
	v_exp_f32_e32 v64, v64
	v_exp_f32_e32 v190, v34
	v_sub_f32_e32 v34, v35, v48
	v_exp_f32_e32 v35, v34
	v_sub_f32_e32 v34, v37, v48
	v_exp_f32_e32 v194, v34
	v_sub_f32_e32 v37, v54, v48
	v_sub_f32_e32 v52, v52, v48
	v_add_f32_e32 v65, v49, v50
	v_exp_f32_e32 v37, v37
	v_exp_f32_e32 v52, v52
	v_sub_f32_e32 v54, v55, v48
	v_sub_f32_e32 v53, v53, v48
	v_add_f32_e32 v65, 0, v65
	v_add_f32_e32 v166, v51, v64
	v_exp_f32_e32 v54, v54
	v_exp_f32_e32 v53, v53
	v_sub_f32_e32 v38, v38, v48
	v_sub_f32_e32 v55, v168, v48
	v_add_f32_e32 v34, v166, v65
	v_add_f32_e32 v36, v167, v190
	v_exp_f32_e32 v38, v38
	v_exp_f32_e32 v55, v55
	v_sub_f32_e32 v39, v39, v48
	v_sub_f32_e32 v65, v169, v48
	v_add_f32_e32 v34, v36, v34
	v_add_f32_e32 v36, v35, v194
	v_exp_f32_e32 v39, v39
	v_exp_f32_e32 v65, v65
	v_sub_f32_e32 v58, v58, v48
	v_sub_f32_e32 v56, v56, v48
	v_add_f32_e32 v34, v36, v34
	v_add_f32_e32 v36, v37, v52
	v_exp_f32_e32 v58, v58
	v_exp_f32_e32 v56, v56
	v_sub_f32_e32 v59, v59, v48
	v_sub_f32_e32 v57, v57, v48
	v_add_f32_e32 v34, v36, v34
	v_add_f32_e32 v36, v54, v53
	v_exp_f32_e32 v59, v59
	v_exp_f32_e32 v57, v57
	v_sub_f32_e32 v40, v40, v48
	v_sub_f32_e32 v42, v42, v48
	v_add_f32_e32 v34, v36, v34
	v_add_f32_e32 v36, v38, v55
	v_exp_f32_e32 v40, v40
	v_exp_f32_e32 v166, v42
	v_sub_f32_e32 v41, v41, v48
	v_sub_f32_e32 v42, v43, v48
	v_add_f32_e32 v34, v36, v34
	v_add_f32_e32 v36, v39, v65
	v_exp_f32_e32 v41, v41
	v_exp_f32_e32 v168, v42
	v_sub_f32_e32 v42, v62, v48
	v_sub_f32_e32 v43, v60, v48
	v_add_f32_e32 v34, v36, v34
	v_add_f32_e32 v36, v58, v56
	v_exp_f32_e32 v42, v42
	v_exp_f32_e32 v60, v43
	v_sub_f32_e32 v43, v63, v48
	v_sub_f32_e32 v61, v61, v48
	v_add_f32_e32 v34, v36, v34
	v_add_f32_e32 v36, v59, v57
	v_exp_f32_e32 v43, v43
	v_exp_f32_e32 v61, v61
	v_sub_f32_e32 v44, v44, v48
	v_sub_f32_e32 v46, v46, v48
	v_add_f32_e32 v34, v36, v34
	v_add_f32_e32 v36, v40, v166
	v_exp_f32_e32 v44, v44
	v_exp_f32_e32 v62, v46
	v_sub_f32_e32 v45, v45, v48
	v_sub_f32_e32 v46, v47, v48
	v_add_f32_e32 v34, v36, v34
	v_add_f32_e32 v36, v41, v168
	v_exp_f32_e32 v45, v45
	v_exp_f32_e32 v63, v46
	v_add_f32_e32 v34, v36, v34
	v_add_f32_e32 v36, v42, v60
	v_add_f32_e32 v34, v36, v34
	v_add_f32_e32 v36, v43, v61
	v_add_f32_e32 v34, v36, v34
	v_add_f32_e32 v36, v44, v62
	v_add_f32_e32 v34, v36, v34
	v_add_f32_e32 v36, v45, v63
	v_add_f32_e32 v192, v36, v34
	v_cvt_pk_bf16_f32 v34, v49, v51
	v_cvt_pk_bf16_f32 v36, v37, v54
	v_cvt_pk_bf16_f32 v37, v38, v39
	v_cvt_pk_bf16_f32 v39, v40, v41
	v_cvt_pk_bf16_f32 v40, v42, v43
	v_cvt_pk_bf16_f32 v42, v50, v64
	ds_read_b64_tr_b16 v[50:51],v171 offset:0
	v_cvt_pk_bf16_f32 v41, v44, v45
	v_cvt_pk_bf16_f32 v44, v52, v53
	ds_read_b64_tr_b16 v[52:53],v171 offset:512
	v_cvt_pk_bf16_f32 v45, v55, v65
	ds_read_b64_tr_b16 v[54:55],v171 offset:1024
	v_cvt_pk_bf16_f32 v46, v56, v57
	ds_read_b64_tr_b16 v[56:57],v171 offset:1536
	v_cvt_pk_bf16_f32 v38, v58, v59
	ds_read_b64_tr_b16 v[58:59],v171 offset:2048
	v_cvt_pk_bf16_f32 v48, v60, v61
	ds_read_b64_tr_b16 v[60:61],v171 offset:2560
	v_cvt_pk_bf16_f32 v49, v62, v63
	ds_read_b64_tr_b16 v[62:63],v171 offset:3072
	ds_read_b64_tr_b16 v[64:65],v171 offset:3584
	v_cvt_pk_bf16_f32 v35, v167, v35
	v_cvt_pk_bf16_f32 v47, v166, v168
	ds_read_b64_tr_b16 v[166:167],v171 offset:4096
	ds_read_b64_tr_b16 v[168:169],v171 offset:4608
	v_cvt_pk_bf16_f32 v43, v190, v194
	ds_read_b64_tr_b16 v[194:195],v171 offset:5120
	ds_read_b64_tr_b16 v[196:197],v171 offset:5632
	ds_read_b64_tr_b16 v[198:199],v171 offset:6144
	ds_read_b64_tr_b16 v[200:201],v171 offset:6656
	ds_read_b64_tr_b16 v[202:203],v171 offset:7168
	ds_read_b64_tr_b16 v[204:205],v171 offset:7680
	s_waitcnt lgkmcnt(8)
	v_fmac_f32_e32 v192, v189, v0
	s_setprio 1
	v_mfma_f32_32x32x16_bf16 v[18:33], v[34:37], v[50:53], v[18:33]
	s_waitcnt lgkmcnt(0)
	v_mfma_f32_32x32x16_bf16 v[18:33], v[38:41], v[54:57], v[18:33]
	v_mfma_f32_32x32x16_bf16 v[18:33], v[42:45], v[58:61], v[18:33]
	v_mfma_f32_32x32x16_bf16 v[18:33], v[46:49], v[62:65], v[18:33]
	v_mfma_f32_32x32x16_bf16 v[2:17], v[34:37], v[166:169], v[2:17]
	s_andn2_b64 vcc, exec, s[0:1]
	v_mfma_f32_32x32x16_bf16 v[2:17], v[38:41], v[194:197], v[2:17]
	v_mfma_f32_32x32x16_bf16 v[2:17], v[42:45], v[198:201], v[2:17]
	v_mfma_f32_32x32x16_bf16 v[2:17], v[46:49], v[202:205], v[2:17]
	s_setprio 0
	s_cbranch_vccnz .LBB0_354
	s_cmp_ge_u32 s87, s86
	s_mov_b64 s[0:1], -1
	s_cbranch_scc0 .LBB0_345
	s_waitcnt vmcnt(0)
	s_mov_b64 s[0:1], 0

.LBB0_347:
	s_setprio 1
	v_mfma_f32_32x32x16_bf16 v[50:65], v[86:89], v[66:69], 0
	v_add_u32_e32 v167, 0xffffffbf, v157
	v_med3_i32 v168, v167, -1, v185
	v_med3_i32 v167, v167, 31, v186
	v_lshl_add_u32 v167, v167, 2, s88
	v_add_u32_e32 v189, 0xffffff84, v167
	v_add_u32_e32 v167, 0xffffffbe, v157
	v_lshl_add_u32 v169, v168, 2, s88
	v_mfma_f32_32x32x16_bf16 v[34:49], v[106:109], v[66:69], 0
	v_med3_i32 v168, v167, -1, v185
	v_med3_i32 v167, v167, 31, v186
	v_lshl_add_u32 v167, v167, 2, s88
	v_subrev_u32_e32 v0, 64, v157
	v_add_u32_e32 v195, 0xffffff84, v167
	v_add_u32_e32 v167, 0xffffffbd, v157
	v_med3_i32 v166, v0, -1, v185
	v_mfma_f32_32x32x16_bf16 v[50:65], v[82:85], v[70:73], v[50:65]
	v_med3_i32 v0, v0, 31, v186
	v_lshl_add_u32 v190, v168, 2, s88
	v_med3_i32 v168, v167, -1, v185
	v_med3_i32 v167, v167, 31, v186
	v_lshl_add_u32 v166, v166, 2, s88
	v_lshl_add_u32 v0, v0, 2, s88
	v_lshl_add_u32 v197, v168, 2, s88
	v_mfma_f32_32x32x16_bf16 v[34:49], v[98:101], v[70:73], v[34:49]
	v_lshl_add_u32 v167, v167, 2, s88
	v_add_u32_e32 v0, 0xffffff84, v0
	v_add_u32_e32 v198, 0xffffff84, v167
	ds_read_b32 v166, v166 offset:4
	ds_read_b32 v168, v0
	ds_read_b32 v167, v169 offset:4
	ds_read_b32 v169, v189
	ds_read_b32 v194, v190 offset:4
	ds_read_b32 v196, v195
	ds_read_b32 v195, v197 offset:4
	ds_read_b32 v197, v198
	v_add_u32_e32 v0, 0xffffffb8, v157
	s_add_i32 s0, s8, 64
	s_cmp_gt_i32 s0, -1
	v_mfma_f32_32x32x16_bf16 v[50:65], v[94:97], v[74:77], v[50:65]
	v_mfma_f32_32x32x16_bf16 v[34:49], v[110:113], v[74:77], v[34:49]
	v_mfma_f32_32x32x16_bf16 v[50:65], v[90:93], v[78:81], v[50:65]
	v_mfma_f32_32x32x16_bf16 v[34:49], v[102:105], v[78:81], v[34:49]
	s_setprio 0
	s_waitcnt lgkmcnt(0)
	s_nop 9
	v_add_f32_e64 v50, v50, v166
	v_add_f32_e64 v51, v51, v167
	v_pk_add_f32 v[166:167], v[34:35], v[168:169]
	v_pk_add_f32 v[34:35], v[52:53], v[194:195]
	v_add_u32_e32 v53, 0xffffffb7, v157
	v_med3_i32 v168, v53, -1, v185
	v_med3_i32 v53, v53, 31, v186
	v_lshl_add_u32 v53, v53, 2, s88
	v_add_u32_e32 v189, 0xffffff84, v53
	v_add_u32_e32 v53, 0xffffffb6, v157
	v_lshl_add_u32 v169, v168, 2, s88
	v_med3_i32 v168, v53, -1, v185
	v_med3_i32 v53, v53, 31, v186
	v_lshl_add_u32 v53, v53, 2, s88
	v_pk_add_f32 v[36:37], v[36:37], v[196:197]
	v_add_u32_e32 v196, 0xffffff84, v53
	v_add_u32_e32 v53, 0xffffffb5, v157
	v_lshl_add_u32 v190, v168, 2, s88
	v_med3_i32 v168, v53, -1, v185
	v_med3_i32 v53, v53, 31, v186
	v_med3_i32 v52, v0, -1, v185
	v_med3_i32 v0, v0, 31, v186
	v_lshl_add_u32 v53, v53, 2, s88
	v_lshl_add_u32 v52, v52, 2, s88
	v_lshl_add_u32 v0, v0, 2, s88
	v_lshl_add_u32 v195, v168, 2, s88
	v_add_u32_e32 v197, 0xffffff84, v53
	v_add_u32_e32 v0, 0xffffff84, v0
	ds_read_b32 v52, v52 offset:4
	ds_read_b32 v168, v0
	ds_read_b32 v53, v169 offset:4
	ds_read_b32 v169, v189
	ds_read_b32 v194, v190 offset:4
	ds_read_b32 v195, v195 offset:4
	ds_read_b32 v196, v196
	ds_read_b32 v197, v197
	s_waitcnt lgkmcnt(0)
	v_pk_add_f32 v[54:55], v[54:55], v[52:53]
	v_pk_add_f32 v[52:53], v[38:39], v[168:169]
	v_pk_add_f32 v[38:39], v[56:57], v[194:195]
	v_add_u32_e32 v57, 0xffffffaf, v157
	v_med3_i32 v168, v57, -1, v185
	v_med3_i32 v57, v57, 31, v186
	v_lshl_add_u32 v57, v57, 2, s88
	v_add_u32_e32 v169, 0xffffff84, v57
	v_add_u32_e32 v57, 0xffffffae, v157
	v_med3_i32 v189, v57, -1, v185
	v_med3_i32 v57, v57, 31, v186
	v_lshl_add_u32 v57, v57, 2, s88
	v_add_u32_e32 v190, 0xffffff84, v57
	v_add_u32_e32 v57, 0xffffffad, v157
	v_add_u32_e32 v0, 0xffffffb0, v157
	v_med3_i32 v194, v57, -1, v185
	v_med3_i32 v57, v57, 31, v186
	v_med3_i32 v56, v0, -1, v185
	v_med3_i32 v0, v0, 31, v186
	v_lshl_add_u32 v57, v57, 2, s88
	v_lshl_add_u32 v56, v56, 2, s88
	v_lshl_add_u32 v0, v0, 2, s88
	v_lshl_add_u32 v199, v194, 2, s88
	v_add_u32_e32 v201, 0xffffff84, v57
	v_add_u32_e32 v0, 0xffffff84, v0
	v_lshl_add_u32 v168, v168, 2, s88
	v_lshl_add_u32 v189, v189, 2, s88
	ds_read_b32 v56, v56 offset:4
	ds_read_b32 v194, v0
	ds_read_b32 v57, v168 offset:4
	ds_read_b32 v195, v169
	ds_read_b32 v198, v189 offset:4
	ds_read_b32 v200, v190
	ds_read_b32 v199, v199 offset:4
	ds_read_b32 v201, v201
	s_waitcnt lgkmcnt(0)
	v_pk_add_f32 v[58:59], v[58:59], v[56:57]
	v_pk_add_f32 v[56:57], v[42:43], v[194:195]
	v_pk_add_f32 v[168:169], v[40:41], v[196:197]
	v_pk_add_f32 v[40:41], v[60:61], v[198:199]
	v_pk_add_f32 v[42:43], v[44:45], v[200:201]
	v_add_u32_e32 v45, 0xffffffa7, v157
	v_med3_i32 v60, v45, -1, v185
	v_med3_i32 v45, v45, 31, v186
	v_lshl_add_u32 v45, v45, 2, s88
	v_add_u32_e32 v189, 0xffffff84, v45
	v_add_u32_e32 v45, 0xffffffa6, v157
	v_lshl_add_u32 v61, v60, 2, s88
	v_med3_i32 v60, v45, -1, v185
	v_med3_i32 v45, v45, 31, v186
	v_lshl_add_u32 v45, v45, 2, s88
	v_add_u32_e32 v196, 0xffffff84, v45
	v_add_u32_e32 v45, 0xffffffa5, v157
	v_add_u32_e32 v0, 0xffffffa8, v157
	v_lshl_add_u32 v190, v60, 2, s88
	v_med3_i32 v60, v45, -1, v185
	v_med3_i32 v45, v45, 31, v186
	v_med3_i32 v44, v0, -1, v185
	v_med3_i32 v0, v0, 31, v186
	v_lshl_add_u32 v45, v45, 2, s88
	v_lshl_add_u32 v44, v44, 2, s88
	v_lshl_add_u32 v0, v0, 2, s88
	v_lshl_add_u32 v195, v60, 2, s88
	v_add_u32_e32 v197, 0xffffff84, v45
	v_add_u32_e32 v0, 0xffffff84, v0
	ds_read_b32 v44, v44 offset:4
	ds_read_b32 v60, v0
	ds_read_b32 v45, v61 offset:4
	ds_read_b32 v61, v189
	ds_read_b32 v194, v190 offset:4
	ds_read_b32 v195, v195 offset:4
	ds_read_b32 v196, v196
	ds_read_b32 v197, v197
	s_waitcnt lgkmcnt(0)
	v_pk_add_f32 v[62:63], v[62:63], v[44:45]
	v_pk_add_f32 v[60:61], v[46:47], v[60:61]
	v_pk_add_f32 v[44:45], v[64:65], v[194:195]
	v_pk_add_f32 v[46:47], v[48:49], v[196:197]
	s_cbranch_scc1 .LBB0_349
	v_add_u32_e32 v0, 64, v191
	v_cmp_lt_i32_e32 vcc, -1, v0
	s_nop 1
	v_cndmask_b32_e32 v50, v187, v50, vcc
	v_cmp_lt_i32_e32 vcc, -2, v0
	s_nop 1
	v_cndmask_b32_e32 v51, v187, v51, vcc
	v_cmp_lt_i32_e32 vcc, -3, v0
	s_nop 1
	v_cndmask_b32_e32 v34, v187, v34, vcc
	v_cmp_lt_i32_e32 vcc, -4, v0
	s_nop 1
	v_cndmask_b32_e32 v35, v187, v35, vcc
	v_cmp_lt_i32_e32 vcc, -9, v0
	s_nop 1
	v_cndmask_b32_e32 v54, v187, v54, vcc
	v_cmp_lt_i32_e32 vcc, -10, v0
	s_nop 1
	v_cndmask_b32_e32 v55, v187, v55, vcc
	v_cmp_lt_i32_e32 vcc, -11, v0
	s_nop 1
	v_cndmask_b32_e32 v38, v187, v38, vcc
	v_cmp_lt_i32_e32 vcc, -12, v0
	s_nop 1
	v_cndmask_b32_e32 v39, v187, v39, vcc
	v_cmp_lt_i32_e32 vcc, s53, v0
	s_nop 1
	v_cndmask_b32_e32 v58, v187, v58, vcc
	v_cmp_lt_i32_e32 vcc, s52, v0
	s_nop 1
	v_cndmask_b32_e32 v59, v187, v59, vcc
	v_cmp_lt_i32_e32 vcc, s51, v0
	s_nop 1
	v_cndmask_b32_e32 v40, v187, v40, vcc
	v_cmp_lt_i32_e32 vcc, s50, v0
	s_nop 1
	v_cndmask_b32_e32 v41, v187, v41, vcc
	v_cmp_lt_i32_e32 vcc, s49, v0
	s_nop 1
	v_cndmask_b32_e32 v62, v187, v62, vcc
	v_cmp_lt_i32_e32 vcc, s48, v0
	s_nop 1
	v_cndmask_b32_e32 v63, v187, v63, vcc
	v_cmp_lt_i32_e32 vcc, s47, v0
	s_nop 1
	v_cndmask_b32_e32 v44, v187, v44, vcc
	v_cmp_lt_i32_e32 vcc, s46, v0
	s_nop 1
	v_cndmask_b32_e32 v45, v187, v45, vcc
	v_cmp_lt_i32_e32 vcc, s70, v0
	s_nop 1
	v_cndmask_b32_e32 v166, v187, v166, vcc
	v_cmp_lt_i32_e32 vcc, s69, v0
	s_nop 1
	v_cndmask_b32_e32 v167, v187, v167, vcc
	v_cmp_lt_i32_e32 vcc, s68, v0
	s_nop 1
	v_cndmask_b32_e32 v36, v187, v36, vcc
	v_cmp_lt_i32_e32 vcc, s67, v0
	s_nop 1
	v_cndmask_b32_e32 v37, v187, v37, vcc
	v_cmp_lt_i32_e32 vcc, s66, v0
	s_nop 1
	v_cndmask_b32_e32 v52, v187, v52, vcc
	v_cmp_lt_i32_e32 vcc, s65, v0
	s_nop 1
	v_cndmask_b32_e32 v53, v187, v53, vcc
	v_cmp_lt_i32_e32 vcc, s64, v0
	s_nop 1
	v_cndmask_b32_e32 v168, v187, v168, vcc
	v_cmp_lt_i32_e32 vcc, s63, v0
	s_nop 1
	v_cndmask_b32_e32 v169, v187, v169, vcc
	v_cmp_lt_i32_e32 vcc, s62, v0
	s_nop 1
	v_cndmask_b32_e32 v56, v187, v56, vcc
	v_cmp_lt_i32_e32 vcc, s61, v0
	s_nop 1
	v_cndmask_b32_e32 v57, v187, v57, vcc
	v_cmp_lt_i32_e32 vcc, s60, v0
	s_nop 1
	v_cndmask_b32_e32 v42, v187, v42, vcc
	v_cmp_lt_i32_e32 vcc, s59, v0
	s_nop 1
	v_cndmask_b32_e32 v43, v187, v43, vcc
	v_cmp_lt_i32_e32 vcc, s58, v0
	s_nop 1
	v_cndmask_b32_e32 v60, v187, v60, vcc
	v_cmp_lt_i32_e32 vcc, s57, v0
	s_nop 1
	v_cndmask_b32_e32 v61, v187, v61, vcc
	v_cmp_lt_i32_e32 vcc, s56, v0
	s_nop 1
	v_cndmask_b32_e32 v46, v187, v46, vcc
	v_cmp_lt_i32_e32 vcc, s55, v0
	s_nop 1
	v_cndmask_b32_e32 v47, v187, v47, vcc

.LBB0_353:
	v_sub_f32_e32 v49, v50, v48
	v_sub_f32_e32 v50, v166, v48
	v_sub_f32_e32 v34, v34, v48
	v_exp_f32_e32 v49, v49
	v_exp_f32_e32 v50, v50
	v_sub_f32_e32 v51, v51, v48
	v_sub_f32_e32 v64, v167, v48
	v_exp_f32_e32 v167, v34
	v_sub_f32_e32 v34, v36, v48
	v_exp_f32_e32 v51, v51
	v_exp_f32_e32 v64, v64
	v_exp_f32_e32 v191, v34
	v_sub_f32_e32 v34, v35, v48
	v_exp_f32_e32 v35, v34
	v_sub_f32_e32 v34, v37, v48
	v_exp_f32_e32 v193, v34
	v_sub_f32_e32 v37, v54, v48
	v_sub_f32_e32 v52, v52, v48
	v_add_f32_e32 v65, v49, v50
	v_exp_f32_e32 v37, v37
	v_exp_f32_e32 v52, v52
	v_sub_f32_e32 v54, v55, v48
	v_sub_f32_e32 v53, v53, v48
	v_add_f32_e32 v65, 0, v65
	v_add_f32_e32 v166, v51, v64
	v_exp_f32_e32 v54, v54
	v_exp_f32_e32 v53, v53
	v_sub_f32_e32 v38, v38, v48
	v_sub_f32_e32 v55, v168, v48
	v_add_f32_e32 v34, v166, v65
	v_add_f32_e32 v36, v167, v191
	v_exp_f32_e32 v38, v38
	v_exp_f32_e32 v55, v55
	v_sub_f32_e32 v39, v39, v48
	v_sub_f32_e32 v65, v169, v48
	v_add_f32_e32 v34, v36, v34
	v_add_f32_e32 v36, v35, v193
	v_exp_f32_e32 v39, v39
	v_exp_f32_e32 v65, v65
	v_sub_f32_e32 v58, v58, v48
	v_sub_f32_e32 v56, v56, v48
	v_add_f32_e32 v34, v36, v34
	v_add_f32_e32 v36, v37, v52
	v_exp_f32_e32 v58, v58
	v_exp_f32_e32 v56, v56
	v_sub_f32_e32 v59, v59, v48
	v_sub_f32_e32 v57, v57, v48
	v_add_f32_e32 v34, v36, v34
	v_add_f32_e32 v36, v54, v53
	v_exp_f32_e32 v59, v59
	v_exp_f32_e32 v57, v57
	v_sub_f32_e32 v40, v40, v48
	v_sub_f32_e32 v42, v42, v48
	v_add_f32_e32 v34, v36, v34
	v_add_f32_e32 v36, v38, v55
	v_exp_f32_e32 v40, v40
	v_exp_f32_e32 v166, v42
	v_sub_f32_e32 v41, v41, v48
	v_sub_f32_e32 v42, v43, v48
	v_add_f32_e32 v34, v36, v34
	v_add_f32_e32 v36, v39, v65
	v_exp_f32_e32 v41, v41
	v_exp_f32_e32 v168, v42
	v_sub_f32_e32 v42, v62, v48
	v_sub_f32_e32 v43, v60, v48
	v_add_f32_e32 v34, v36, v34
	v_add_f32_e32 v36, v58, v56
	v_exp_f32_e32 v42, v42
	v_exp_f32_e32 v60, v43
	v_sub_f32_e32 v43, v63, v48
	v_sub_f32_e32 v61, v61, v48
	v_add_f32_e32 v34, v36, v34
	v_add_f32_e32 v36, v59, v57
	v_exp_f32_e32 v43, v43
	v_exp_f32_e32 v61, v61
	v_sub_f32_e32 v44, v44, v48
	v_sub_f32_e32 v46, v46, v48
	v_add_f32_e32 v34, v36, v34
	v_add_f32_e32 v36, v40, v166
	v_exp_f32_e32 v44, v44
	v_exp_f32_e32 v62, v46
	v_sub_f32_e32 v45, v45, v48
	v_sub_f32_e32 v46, v47, v48
	v_add_f32_e32 v34, v36, v34
	v_add_f32_e32 v36, v41, v168
	v_exp_f32_e32 v45, v45
	v_exp_f32_e32 v63, v46
	v_add_f32_e32 v34, v36, v34
	v_add_f32_e32 v36, v42, v60
	v_add_f32_e32 v34, v36, v34
	v_add_f32_e32 v36, v43, v61
	v_add_f32_e32 v34, v36, v34
	v_add_f32_e32 v36, v44, v62
	v_add_f32_e32 v34, v36, v34
	v_add_f32_e32 v36, v45, v63
	v_add_f32_e32 v189, v36, v34
	v_cvt_pk_bf16_f32 v34, v49, v51
	v_cvt_pk_bf16_f32 v36, v37, v54
	v_cvt_pk_bf16_f32 v37, v38, v39
	v_cvt_pk_bf16_f32 v39, v40, v41
	v_cvt_pk_bf16_f32 v40, v42, v43
	v_cvt_pk_bf16_f32 v42, v50, v64
	ds_read_b64_tr_b16 v[50:51],v181 offset:0
	v_cvt_pk_bf16_f32 v41, v44, v45
	v_cvt_pk_bf16_f32 v44, v52, v53
	ds_read_b64_tr_b16 v[52:53],v181 offset:512
	v_cvt_pk_bf16_f32 v45, v55, v65
	ds_read_b64_tr_b16 v[54:55],v181 offset:1024
	v_cvt_pk_bf16_f32 v46, v56, v57
	ds_read_b64_tr_b16 v[56:57],v181 offset:1536
	v_cvt_pk_bf16_f32 v38, v58, v59
	ds_read_b64_tr_b16 v[58:59],v181 offset:2048
	v_cvt_pk_bf16_f32 v48, v60, v61
	ds_read_b64_tr_b16 v[60:61],v181 offset:2560
	v_cvt_pk_bf16_f32 v49, v62, v63
	ds_read_b64_tr_b16 v[62:63],v181 offset:3072
	ds_read_b64_tr_b16 v[64:65],v181 offset:3584
	v_cvt_pk_bf16_f32 v35, v167, v35
	v_cvt_pk_bf16_f32 v47, v166, v168
	ds_read_b64_tr_b16 v[166:167],v181 offset:4096
	ds_read_b64_tr_b16 v[168:169],v181 offset:4608
	v_fmac_f32_e32 v189, v192, v0
	v_cvt_pk_bf16_f32 v43, v191, v193
	ds_read_b64_tr_b16 v[192:193],v181 offset:5120
	ds_read_b64_tr_b16 v[194:195],v181 offset:5632
	ds_read_b64_tr_b16 v[196:197],v181 offset:6144
	ds_read_b64_tr_b16 v[198:199],v181 offset:6656
	ds_read_b64_tr_b16 v[200:201],v181 offset:7168
	ds_read_b64_tr_b16 v[202:203],v181 offset:7680
	s_waitcnt lgkmcnt(8)
	s_setprio 1
	v_mfma_f32_32x32x16_bf16 v[18:33], v[34:37], v[50:53], v[18:33]
	s_waitcnt lgkmcnt(0)
	v_mfma_f32_32x32x16_bf16 v[18:33], v[38:41], v[54:57], v[18:33]
	v_mfma_f32_32x32x16_bf16 v[18:33], v[42:45], v[58:61], v[18:33]
	v_mfma_f32_32x32x16_bf16 v[18:33], v[46:49], v[62:65], v[18:33]
	v_mfma_f32_32x32x16_bf16 v[2:17], v[34:37], v[166:169], v[2:17]
	v_mfma_f32_32x32x16_bf16 v[2:17], v[38:41], v[192:195], v[2:17]
	v_mfma_f32_32x32x16_bf16 v[2:17], v[42:45], v[196:199], v[2:17]
	v_mfma_f32_32x32x16_bf16 v[2:17], v[46:49], v[200:203], v[2:17]
	s_setprio 0
	s_branch .LBB0_355
